# as the Q-in-registers version, plus waves 4-7 take the per-tile barrier in front of the last QK^T MFMA pair (all LDS reads done there) in the differential-attention loops
# baseline (speedup 1.0000x reference)
.LBB0_557:
	ds_read_b64_tr_b16 v[144:145], v177 offset:0
	ds_read_b64_tr_b16 v[146:147], v177 offset:0x1000
	ds_read_b64_tr_b16 v[148:149], v177 offset:0x2000
	ds_read_b64_tr_b16 v[150:151], v177 offset:0x3000
	ds_read_b64_tr_b16 v[152:153], v177 offset:0x4000
	ds_read_b64_tr_b16 v[154:155], v177 offset:0x5000
	ds_read_b64_tr_b16 v[156:157], v177 offset:0x6000
	ds_read_b64_tr_b16 v[158:159], v177 offset:0x7000
	s_waitcnt lgkmcnt(6)
	s_nop 0
	v_mfma_f32_32x32x16_bf16 v[112:127], v[144:147], v[128:131], v[112:127]
	ds_read_b64_tr_b16 v[192:193], v177 offset:0x200
	ds_read_b64_tr_b16 v[194:195], v177 offset:0x1200
	s_waitcnt lgkmcnt(6)
	v_mfma_f32_32x32x16_bf16 v[112:127], v[148:151], v[132:135], v[112:127]
	ds_read_b64_tr_b16 v[196:197], v177 offset:0x2200
	ds_read_b64_tr_b16 v[198:199], v177 offset:0x3200
	s_waitcnt lgkmcnt(6)
	v_mfma_f32_32x32x16_bf16 v[112:127], v[152:155], v[136:139], v[112:127]
	ds_read_b64_tr_b16 v[200:201], v177 offset:0x4200
	ds_read_b64_tr_b16 v[202:203], v177 offset:0x5200
	s_waitcnt lgkmcnt(6)
	v_mfma_f32_32x32x16_bf16 v[112:127], v[156:159], v[140:143], v[112:127]
	ds_read_b64_tr_b16 v[204:205], v177 offset:0x6200
	ds_read_b64_tr_b16 v[206:207], v177 offset:0x7200
	s_waitcnt lgkmcnt(6)
	v_mfma_f32_32x32x16_bf16 v[80:95], v[192:195], v[128:131], v[80:95]
	ds_read_b64_tr_b16 v[144:145], v177 offset:0x400
	ds_read_b64_tr_b16 v[146:147], v177 offset:0x1400
	s_waitcnt lgkmcnt(6)
	v_mfma_f32_32x32x16_bf16 v[80:95], v[196:199], v[132:135], v[80:95]
	ds_read_b64_tr_b16 v[148:149], v177 offset:0x2400
	ds_read_b64_tr_b16 v[150:151], v177 offset:0x3400
	s_waitcnt lgkmcnt(6)
	v_mfma_f32_32x32x16_bf16 v[80:95], v[200:203], v[136:139], v[80:95]
	ds_read_b64_tr_b16 v[152:153], v177 offset:0x4400
	ds_read_b64_tr_b16 v[154:155], v177 offset:0x5400
	s_waitcnt lgkmcnt(6)
	v_mfma_f32_32x32x16_bf16 v[80:95], v[204:207], v[140:143], v[80:95]
	ds_read_b64_tr_b16 v[156:157], v177 offset:0x6400
	ds_read_b64_tr_b16 v[158:159], v177 offset:0x7400
	s_waitcnt lgkmcnt(6)
	v_mfma_f32_32x32x16_bf16 v[96:111], v[144:147], v[128:131], v[96:111]
	ds_read_b64_tr_b16 v[192:193], v177 offset:0x600
	ds_read_b64_tr_b16 v[194:195], v177 offset:0x1600
	s_waitcnt lgkmcnt(6)
	v_mfma_f32_32x32x16_bf16 v[96:111], v[148:151], v[132:135], v[96:111]
	ds_read_b64_tr_b16 v[196:197], v177 offset:0x2600
	ds_read_b64_tr_b16 v[198:199], v177 offset:0x3600
	s_waitcnt lgkmcnt(6)
	v_mfma_f32_32x32x16_bf16 v[96:111], v[152:155], v[136:139], v[96:111]
	ds_read_b64_tr_b16 v[200:201], v177 offset:0x4600
	ds_read_b64_tr_b16 v[202:203], v177 offset:0x5600
	s_waitcnt lgkmcnt(6)
	v_mfma_f32_32x32x16_bf16 v[96:111], v[156:159], v[140:143], v[96:111]
	ds_read_b64_tr_b16 v[204:205], v177 offset:0x6600
	ds_read_b64_tr_b16 v[206:207], v177 offset:0x7600
	s_waitcnt lgkmcnt(6)
	v_mfma_f32_32x32x16_bf16 v[64:79], v[192:195], v[128:131], v[64:79]
	ds_read_b64_tr_b16 v[144:145], v177 offset:0x800
	ds_read_b64_tr_b16 v[146:147], v177 offset:0x1800
	s_waitcnt lgkmcnt(6)
	v_mfma_f32_32x32x16_bf16 v[64:79], v[196:199], v[132:135], v[64:79]
	ds_read_b64_tr_b16 v[148:149], v177 offset:0x2800
	ds_read_b64_tr_b16 v[150:151], v177 offset:0x3800
	s_waitcnt lgkmcnt(6)
	v_mfma_f32_32x32x16_bf16 v[64:79], v[200:203], v[136:139], v[64:79]
	ds_read_b64_tr_b16 v[152:153], v177 offset:0x4800
	ds_read_b64_tr_b16 v[154:155], v177 offset:0x5800
	s_waitcnt lgkmcnt(6)
	v_mfma_f32_32x32x16_bf16 v[64:79], v[204:207], v[140:143], v[64:79]
	ds_read_b64_tr_b16 v[156:157], v177 offset:0x6800
	ds_read_b64_tr_b16 v[158:159], v177 offset:0x7800
	s_waitcnt lgkmcnt(6)
	v_mfma_f32_32x32x16_bf16 v[48:63], v[144:147], v[128:131], v[48:63]
	ds_read_b64_tr_b16 v[192:193], v177 offset:0xa00
	ds_read_b64_tr_b16 v[194:195], v177 offset:0x1a00
	s_waitcnt lgkmcnt(6)
	v_mfma_f32_32x32x16_bf16 v[48:63], v[148:151], v[132:135], v[48:63]
	ds_read_b64_tr_b16 v[196:197], v177 offset:0x2a00
	ds_read_b64_tr_b16 v[198:199], v177 offset:0x3a00
	s_waitcnt lgkmcnt(6)
	v_mfma_f32_32x32x16_bf16 v[48:63], v[152:155], v[136:139], v[48:63]
	ds_read_b64_tr_b16 v[200:201], v177 offset:0x4a00
	ds_read_b64_tr_b16 v[202:203], v177 offset:0x5a00
	s_waitcnt lgkmcnt(6)
	v_mfma_f32_32x32x16_bf16 v[48:63], v[156:159], v[140:143], v[48:63]
	ds_read_b64_tr_b16 v[204:205], v177 offset:0x6a00
	ds_read_b64_tr_b16 v[206:207], v177 offset:0x7a00
	s_waitcnt lgkmcnt(6)
	v_mfma_f32_32x32x16_bf16 v[32:47], v[192:195], v[128:131], v[32:47]
	ds_read_b64_tr_b16 v[144:145], v177 offset:0xc00
	ds_read_b64_tr_b16 v[146:147], v177 offset:0x1c00
	s_waitcnt lgkmcnt(6)
	v_mfma_f32_32x32x16_bf16 v[32:47], v[196:199], v[132:135], v[32:47]
	ds_read_b64_tr_b16 v[148:149], v177 offset:0x2c00
	ds_read_b64_tr_b16 v[150:151], v177 offset:0x3c00
	s_waitcnt lgkmcnt(6)
	v_mfma_f32_32x32x16_bf16 v[32:47], v[200:203], v[136:139], v[32:47]
	ds_read_b64_tr_b16 v[152:153], v177 offset:0x4c00
	ds_read_b64_tr_b16 v[154:155], v177 offset:0x5c00
	s_waitcnt lgkmcnt(6)
	v_mfma_f32_32x32x16_bf16 v[32:47], v[204:207], v[140:143], v[32:47]
	ds_read_b64_tr_b16 v[156:157], v177 offset:0x6c00
	ds_read_b64_tr_b16 v[158:159], v177 offset:0x7c00
	s_waitcnt lgkmcnt(6)
	v_mfma_f32_32x32x16_bf16 v[16:31], v[144:147], v[128:131], v[16:31]
	ds_read_b64_tr_b16 v[192:193], v177 offset:0xe00
	ds_read_b64_tr_b16 v[194:195], v177 offset:0x1e00
	s_waitcnt lgkmcnt(6)
	v_mfma_f32_32x32x16_bf16 v[16:31], v[148:151], v[132:135], v[16:31]
	ds_read_b64_tr_b16 v[196:197], v177 offset:0x2e00
	ds_read_b64_tr_b16 v[198:199], v177 offset:0x3e00
	s_waitcnt lgkmcnt(6)
	v_mfma_f32_32x32x16_bf16 v[16:31], v[152:155], v[136:139], v[16:31]
	ds_read_b64_tr_b16 v[200:201], v177 offset:0x4e00
	ds_read_b64_tr_b16 v[202:203], v177 offset:0x5e00
	s_waitcnt lgkmcnt(6)
	v_mfma_f32_32x32x16_bf16 v[16:31], v[156:159], v[140:143], v[16:31]
	ds_read_b64_tr_b16 v[204:205], v177 offset:0x6e00
	ds_read_b64_tr_b16 v[206:207], v177 offset:0x7e00
	s_waitcnt lgkmcnt(6)
	v_mfma_f32_32x32x16_bf16 v[0:15], v[192:195], v[128:131], v[0:15]
	s_waitcnt lgkmcnt(4)
	v_mfma_f32_32x32x16_bf16 v[0:15], v[196:199], v[132:135], v[0:15]
	s_waitcnt lgkmcnt(2)
	v_mfma_f32_32x32x16_bf16 v[0:15], v[200:203], v[136:139], v[0:15]
	s_waitcnt lgkmcnt(0)
	v_mfma_f32_32x32x16_bf16 v[0:15], v[204:207], v[140:143], v[0:15]
	ds_read_b128 v[128:131], v188 offset:0
	ds_read_b128 v[132:135], v188 offset:0x2000
	ds_read_b128 v[192:195], v187 offset:0
	ds_read_b128 v[196:199], v187 offset:0x2000
	s_waitcnt lgkmcnt(2)
	s_nop 0
	v_mfma_f32_32x32x16_bf16 v[144:159], v[128:131], v[218:221], 0
	v_mfma_f32_32x32x16_bf16 v[128:143], v[132:135], v[218:221], 0
	ds_read_b128 v[204:207], v186 offset:0
	ds_read_b128 v[208:211], v186 offset:0x2000
	s_waitcnt lgkmcnt(2)
	v_mfma_f32_32x32x16_bf16 v[144:159], v[192:195], v[222:225], v[144:159]
	v_mfma_f32_32x32x16_bf16 v[128:143], v[196:199], v[222:225], v[128:143]
	ds_read_b128 v[192:195], v185 offset:0
	ds_read_b128 v[196:199], v185 offset:0x2000
	s_waitcnt lgkmcnt(2)
	v_mfma_f32_32x32x16_bf16 v[144:159], v[204:207], v[230:233], v[144:159]
	v_mfma_f32_32x32x16_bf16 v[128:143], v[208:211], v[230:233], v[128:143]
	ds_read_b128 v[204:207], v188 offset:0x80
	ds_read_b128 v[208:211], v188 offset:0x2080
	s_waitcnt lgkmcnt(2)
	v_mfma_f32_32x32x16_bf16 v[144:159], v[192:195], v[234:237], v[144:159]
	v_mfma_f32_32x32x16_bf16 v[128:143], v[196:199], v[234:237], v[128:143]
	ds_read_b128 v[192:195], v187 offset:0x80
	ds_read_b128 v[196:199], v187 offset:0x2080
	s_waitcnt lgkmcnt(2)
	v_mfma_f32_32x32x16_bf16 v[144:159], v[204:207], v[238:241], v[144:159]
	v_mfma_f32_32x32x16_bf16 v[128:143], v[208:211], v[238:241], v[128:143]
	ds_read_b128 v[204:207], v186 offset:0x80
	ds_read_b128 v[208:211], v186 offset:0x2080
	s_waitcnt lgkmcnt(2)
	v_mfma_f32_32x32x16_bf16 v[144:159], v[192:195], v[242:245], v[144:159]
	v_mfma_f32_32x32x16_bf16 v[128:143], v[196:199], v[242:245], v[128:143]
	ds_read_b128 v[192:195], v185 offset:0x80
	ds_read_b128 v[196:199], v185 offset:0x2080
	s_waitcnt lgkmcnt(2)
	v_mfma_f32_32x32x16_bf16 v[144:159], v[204:207], v[246:249], v[144:159]
	v_mfma_f32_32x32x16_bf16 v[128:143], v[208:211], v[246:249], v[128:143]
	s_waitcnt lgkmcnt(0)
	s_bitcmp0_b32 s100, 8
	s_cbranch_scc1 .Lqk7bar_0
	s_waitcnt vmcnt(0)
	s_barrier
.Lqk7bar_0:
	v_mfma_f32_32x32x16_bf16 v[144:159], v[192:195], v[166:169], v[144:159]
	v_mfma_f32_32x32x16_bf16 v[128:143], v[196:199], v[166:169], v[128:143]
	s_bitcmp0_b32 s100, 8
	s_cbranch_scc1 .Lstg_a10
	s_sleep 5

.LBB0_565:
	ds_read_b64_tr_b16 v[144:145], v177 offset:0x8000
	ds_read_b64_tr_b16 v[146:147], v177 offset:0x9000
	ds_read_b64_tr_b16 v[148:149], v177 offset:0xa000
	ds_read_b64_tr_b16 v[150:151], v177 offset:0xb000
	ds_read_b64_tr_b16 v[152:153], v177 offset:0xc000
	ds_read_b64_tr_b16 v[154:155], v177 offset:0xd000
	ds_read_b64_tr_b16 v[156:157], v177 offset:0xe000
	ds_read_b64_tr_b16 v[158:159], v177 offset:0xf000
	s_waitcnt lgkmcnt(6)
	s_nop 0
	v_mfma_f32_32x32x16_bf16 v[112:127], v[144:147], v[128:131], v[112:127]
	ds_read_b64_tr_b16 v[194:195], v177 offset:0x8200
	ds_read_b64_tr_b16 v[196:197], v177 offset:0x9200
	s_waitcnt lgkmcnt(6)
	v_mfma_f32_32x32x16_bf16 v[112:127], v[148:151], v[132:135], v[112:127]
	ds_read_b64_tr_b16 v[198:199], v177 offset:0xa200
	ds_read_b64_tr_b16 v[200:201], v177 offset:0xb200
	s_waitcnt lgkmcnt(6)
	v_mfma_f32_32x32x16_bf16 v[112:127], v[152:155], v[136:139], v[112:127]
	ds_read_b64_tr_b16 v[202:203], v177 offset:0xc200
	ds_read_b64_tr_b16 v[204:205], v177 offset:0xd200
	s_waitcnt lgkmcnt(6)
	v_mfma_f32_32x32x16_bf16 v[112:127], v[156:159], v[140:143], v[112:127]
	ds_read_b64_tr_b16 v[206:207], v177 offset:0xe200
	ds_read_b64_tr_b16 v[208:209], v177 offset:0xf200
	s_waitcnt lgkmcnt(6)
	v_mfma_f32_32x32x16_bf16 v[80:95], v[194:197], v[128:131], v[80:95]
	ds_read_b64_tr_b16 v[144:145], v177 offset:0x8400
	ds_read_b64_tr_b16 v[146:147], v177 offset:0x9400
	s_waitcnt lgkmcnt(6)
	v_mfma_f32_32x32x16_bf16 v[80:95], v[198:201], v[132:135], v[80:95]
	ds_read_b64_tr_b16 v[148:149], v177 offset:0xa400
	ds_read_b64_tr_b16 v[150:151], v177 offset:0xb400
	s_waitcnt lgkmcnt(6)
	v_mfma_f32_32x32x16_bf16 v[80:95], v[202:205], v[136:139], v[80:95]
	ds_read_b64_tr_b16 v[152:153], v177 offset:0xc400
	ds_read_b64_tr_b16 v[154:155], v177 offset:0xd400
	s_waitcnt lgkmcnt(6)
	v_mfma_f32_32x32x16_bf16 v[80:95], v[206:209], v[140:143], v[80:95]
	ds_read_b64_tr_b16 v[156:157], v177 offset:0xe400
	ds_read_b64_tr_b16 v[158:159], v177 offset:0xf400
	s_waitcnt lgkmcnt(6)
	v_mfma_f32_32x32x16_bf16 v[96:111], v[144:147], v[128:131], v[96:111]
	ds_read_b64_tr_b16 v[194:195], v177 offset:0x8600
	ds_read_b64_tr_b16 v[196:197], v177 offset:0x9600
	s_waitcnt lgkmcnt(6)
	v_mfma_f32_32x32x16_bf16 v[96:111], v[148:151], v[132:135], v[96:111]
	ds_read_b64_tr_b16 v[198:199], v177 offset:0xa600
	ds_read_b64_tr_b16 v[200:201], v177 offset:0xb600
	s_waitcnt lgkmcnt(6)
	v_mfma_f32_32x32x16_bf16 v[96:111], v[152:155], v[136:139], v[96:111]
	ds_read_b64_tr_b16 v[202:203], v177 offset:0xc600
	ds_read_b64_tr_b16 v[204:205], v177 offset:0xd600
	s_waitcnt lgkmcnt(6)
	v_mfma_f32_32x32x16_bf16 v[96:111], v[156:159], v[140:143], v[96:111]
	ds_read_b64_tr_b16 v[206:207], v177 offset:0xe600
	ds_read_b64_tr_b16 v[208:209], v177 offset:0xf600
	s_waitcnt lgkmcnt(6)
	v_mfma_f32_32x32x16_bf16 v[64:79], v[194:197], v[128:131], v[64:79]
	ds_read_b64_tr_b16 v[144:145], v177 offset:0x8800
	ds_read_b64_tr_b16 v[146:147], v177 offset:0x9800
	s_waitcnt lgkmcnt(6)
	v_mfma_f32_32x32x16_bf16 v[64:79], v[198:201], v[132:135], v[64:79]
	ds_read_b64_tr_b16 v[148:149], v177 offset:0xa800
	ds_read_b64_tr_b16 v[150:151], v177 offset:0xb800
	s_waitcnt lgkmcnt(6)
	v_mfma_f32_32x32x16_bf16 v[64:79], v[202:205], v[136:139], v[64:79]
	ds_read_b64_tr_b16 v[152:153], v177 offset:0xc800
	ds_read_b64_tr_b16 v[154:155], v177 offset:0xd800
	s_waitcnt lgkmcnt(6)
	v_mfma_f32_32x32x16_bf16 v[64:79], v[206:209], v[140:143], v[64:79]
	ds_read_b64_tr_b16 v[156:157], v177 offset:0xe800
	ds_read_b64_tr_b16 v[158:159], v177 offset:0xf800
	s_waitcnt lgkmcnt(6)
	v_mfma_f32_32x32x16_bf16 v[48:63], v[144:147], v[128:131], v[48:63]
	ds_read_b64_tr_b16 v[194:195], v177 offset:0x8a00
	ds_read_b64_tr_b16 v[196:197], v177 offset:0x9a00
	s_waitcnt lgkmcnt(6)
	v_mfma_f32_32x32x16_bf16 v[48:63], v[148:151], v[132:135], v[48:63]
	ds_read_b64_tr_b16 v[198:199], v177 offset:0xaa00
	ds_read_b64_tr_b16 v[200:201], v177 offset:0xba00
	s_waitcnt lgkmcnt(6)
	v_mfma_f32_32x32x16_bf16 v[48:63], v[152:155], v[136:139], v[48:63]
	ds_read_b64_tr_b16 v[202:203], v177 offset:0xca00
	ds_read_b64_tr_b16 v[204:205], v177 offset:0xda00
	s_waitcnt lgkmcnt(6)
	v_mfma_f32_32x32x16_bf16 v[48:63], v[156:159], v[140:143], v[48:63]
	ds_read_b64_tr_b16 v[206:207], v177 offset:0xea00
	ds_read_b64_tr_b16 v[208:209], v177 offset:0xfa00
	s_waitcnt lgkmcnt(6)
	v_mfma_f32_32x32x16_bf16 v[32:47], v[194:197], v[128:131], v[32:47]
	ds_read_b64_tr_b16 v[144:145], v177 offset:0x8c00
	ds_read_b64_tr_b16 v[146:147], v177 offset:0x9c00
	s_waitcnt lgkmcnt(6)
	v_mfma_f32_32x32x16_bf16 v[32:47], v[198:201], v[132:135], v[32:47]
	ds_read_b64_tr_b16 v[148:149], v177 offset:0xac00
	ds_read_b64_tr_b16 v[150:151], v177 offset:0xbc00
	s_waitcnt lgkmcnt(6)
	v_mfma_f32_32x32x16_bf16 v[32:47], v[202:205], v[136:139], v[32:47]
	ds_read_b64_tr_b16 v[152:153], v177 offset:0xcc00
	ds_read_b64_tr_b16 v[154:155], v177 offset:0xdc00
	s_waitcnt lgkmcnt(6)
	v_mfma_f32_32x32x16_bf16 v[32:47], v[206:209], v[140:143], v[32:47]
	ds_read_b64_tr_b16 v[156:157], v177 offset:0xec00
	ds_read_b64_tr_b16 v[158:159], v177 offset:0xfc00
	s_waitcnt lgkmcnt(6)
	v_mfma_f32_32x32x16_bf16 v[16:31], v[144:147], v[128:131], v[16:31]
	ds_read_b64_tr_b16 v[194:195], v177 offset:0x8e00
	ds_read_b64_tr_b16 v[196:197], v177 offset:0x9e00
	s_waitcnt lgkmcnt(6)
	v_mfma_f32_32x32x16_bf16 v[16:31], v[148:151], v[132:135], v[16:31]
	ds_read_b64_tr_b16 v[198:199], v177 offset:0xae00
	ds_read_b64_tr_b16 v[200:201], v177 offset:0xbe00
	s_waitcnt lgkmcnt(6)
	v_mfma_f32_32x32x16_bf16 v[16:31], v[152:155], v[136:139], v[16:31]
	ds_read_b64_tr_b16 v[202:203], v177 offset:0xce00
	ds_read_b64_tr_b16 v[204:205], v177 offset:0xde00
	s_waitcnt lgkmcnt(6)
	v_mfma_f32_32x32x16_bf16 v[16:31], v[156:159], v[140:143], v[16:31]
	ds_read_b64_tr_b16 v[206:207], v177 offset:0xee00
	ds_read_b64_tr_b16 v[208:209], v177 offset:0xfe00
	s_waitcnt lgkmcnt(6)
	v_mfma_f32_32x32x16_bf16 v[0:15], v[194:197], v[128:131], v[0:15]
	s_waitcnt lgkmcnt(4)
	v_mfma_f32_32x32x16_bf16 v[0:15], v[198:201], v[132:135], v[0:15]
	s_waitcnt lgkmcnt(2)
	v_mfma_f32_32x32x16_bf16 v[0:15], v[202:205], v[136:139], v[0:15]
	s_waitcnt lgkmcnt(0)
	v_mfma_f32_32x32x16_bf16 v[0:15], v[206:209], v[140:143], v[0:15]
	ds_read_b128 v[128:131], v181 offset:0
	ds_read_b128 v[132:135], v181 offset:0x2000
	ds_read_b128 v[194:197], v182 offset:0
	ds_read_b128 v[198:201], v182 offset:0x2000
	s_waitcnt lgkmcnt(2)
	s_nop 0
	v_mfma_f32_32x32x16_bf16 v[144:159], v[128:131], v[218:221], 0
	v_mfma_f32_32x32x16_bf16 v[128:143], v[132:135], v[218:221], 0
	ds_read_b128 v[206:209], v183 offset:0
	ds_read_b128 v[210:213], v183 offset:0x2000
	s_waitcnt lgkmcnt(2)
	v_mfma_f32_32x32x16_bf16 v[144:159], v[194:197], v[222:225], v[144:159]
	v_mfma_f32_32x32x16_bf16 v[128:143], v[198:201], v[222:225], v[128:143]
	ds_read_b128 v[194:197], v184 offset:0
	ds_read_b128 v[198:201], v184 offset:0x2000
	s_waitcnt lgkmcnt(2)
	v_mfma_f32_32x32x16_bf16 v[144:159], v[206:209], v[230:233], v[144:159]
	v_mfma_f32_32x32x16_bf16 v[128:143], v[210:213], v[230:233], v[128:143]
	ds_read_b128 v[206:209], v181 offset:0x80
	ds_read_b128 v[210:213], v181 offset:0x2080
	s_waitcnt lgkmcnt(2)
	v_mfma_f32_32x32x16_bf16 v[144:159], v[194:197], v[234:237], v[144:159]
	v_mfma_f32_32x32x16_bf16 v[128:143], v[198:201], v[234:237], v[128:143]
	ds_read_b128 v[194:197], v182 offset:0x80
	ds_read_b128 v[198:201], v182 offset:0x2080
	s_waitcnt lgkmcnt(2)
	v_mfma_f32_32x32x16_bf16 v[144:159], v[206:209], v[238:241], v[144:159]
	v_mfma_f32_32x32x16_bf16 v[128:143], v[210:213], v[238:241], v[128:143]
	ds_read_b128 v[206:209], v183 offset:0x80
	ds_read_b128 v[210:213], v183 offset:0x2080
	s_waitcnt lgkmcnt(2)
	v_mfma_f32_32x32x16_bf16 v[144:159], v[194:197], v[242:245], v[144:159]
	v_mfma_f32_32x32x16_bf16 v[128:143], v[198:201], v[242:245], v[128:143]
	ds_read_b128 v[194:197], v184 offset:0x80
	ds_read_b128 v[198:201], v184 offset:0x2080
	s_waitcnt lgkmcnt(2)
	v_mfma_f32_32x32x16_bf16 v[144:159], v[206:209], v[246:249], v[144:159]
	v_mfma_f32_32x32x16_bf16 v[128:143], v[210:213], v[246:249], v[128:143]
	s_waitcnt lgkmcnt(0)
	s_bitcmp0_b32 s100, 8
	s_cbranch_scc1 .Lqk7bar_1
	s_waitcnt vmcnt(0)
	s_barrier
.Lqk7bar_1:
	v_mfma_f32_32x32x16_bf16 v[144:159], v[194:197], v[166:169], v[144:159]
	v_mfma_f32_32x32x16_bf16 v[128:143], v[198:201], v[166:169], v[128:143]
	s_bitcmp0_b32 s100, 8
	s_cbranch_scc1 .Lstg_a11
	s_sleep 5

.LBB0_589:
	ds_read_b64_tr_b16 v[144:145], v177 offset:0
	ds_read_b64_tr_b16 v[146:147], v177 offset:0x1000
	ds_read_b64_tr_b16 v[148:149], v177 offset:0x2000
	ds_read_b64_tr_b16 v[150:151], v177 offset:0x3000
	ds_read_b64_tr_b16 v[152:153], v177 offset:0x4000
	ds_read_b64_tr_b16 v[154:155], v177 offset:0x5000
	ds_read_b64_tr_b16 v[156:157], v177 offset:0x6000
	ds_read_b64_tr_b16 v[158:159], v177 offset:0x7000
	s_waitcnt lgkmcnt(6)
	s_nop 0
	v_mfma_f32_32x32x16_bf16 v[112:127], v[144:147], v[128:131], v[112:127]
	ds_read_b64_tr_b16 v[192:193], v177 offset:0x200
	ds_read_b64_tr_b16 v[194:195], v177 offset:0x1200
	s_waitcnt lgkmcnt(6)
	v_mfma_f32_32x32x16_bf16 v[112:127], v[148:151], v[132:135], v[112:127]
	ds_read_b64_tr_b16 v[196:197], v177 offset:0x2200
	ds_read_b64_tr_b16 v[198:199], v177 offset:0x3200
	s_waitcnt lgkmcnt(6)
	v_mfma_f32_32x32x16_bf16 v[112:127], v[152:155], v[136:139], v[112:127]
	ds_read_b64_tr_b16 v[200:201], v177 offset:0x4200
	ds_read_b64_tr_b16 v[202:203], v177 offset:0x5200
	s_waitcnt lgkmcnt(6)
	v_mfma_f32_32x32x16_bf16 v[112:127], v[156:159], v[140:143], v[112:127]
	ds_read_b64_tr_b16 v[204:205], v177 offset:0x6200
	ds_read_b64_tr_b16 v[206:207], v177 offset:0x7200
	s_waitcnt lgkmcnt(6)
	v_mfma_f32_32x32x16_bf16 v[96:111], v[192:195], v[128:131], v[96:111]
	ds_read_b64_tr_b16 v[144:145], v177 offset:0x400
	ds_read_b64_tr_b16 v[146:147], v177 offset:0x1400
	s_waitcnt lgkmcnt(6)
	v_mfma_f32_32x32x16_bf16 v[96:111], v[196:199], v[132:135], v[96:111]
	ds_read_b64_tr_b16 v[148:149], v177 offset:0x2400
	ds_read_b64_tr_b16 v[150:151], v177 offset:0x3400
	s_waitcnt lgkmcnt(6)
	v_mfma_f32_32x32x16_bf16 v[96:111], v[200:203], v[136:139], v[96:111]
	ds_read_b64_tr_b16 v[152:153], v177 offset:0x4400
	ds_read_b64_tr_b16 v[154:155], v177 offset:0x5400
	s_waitcnt lgkmcnt(6)
	v_mfma_f32_32x32x16_bf16 v[96:111], v[204:207], v[140:143], v[96:111]
	ds_read_b64_tr_b16 v[156:157], v177 offset:0x6400
	ds_read_b64_tr_b16 v[158:159], v177 offset:0x7400
	s_waitcnt lgkmcnt(6)
	v_mfma_f32_32x32x16_bf16 v[80:95], v[144:147], v[128:131], v[80:95]
	ds_read_b64_tr_b16 v[192:193], v177 offset:0x600
	ds_read_b64_tr_b16 v[194:195], v177 offset:0x1600
	s_waitcnt lgkmcnt(6)
	v_mfma_f32_32x32x16_bf16 v[80:95], v[148:151], v[132:135], v[80:95]
	ds_read_b64_tr_b16 v[196:197], v177 offset:0x2600
	ds_read_b64_tr_b16 v[198:199], v177 offset:0x3600
	s_waitcnt lgkmcnt(6)
	v_mfma_f32_32x32x16_bf16 v[80:95], v[152:155], v[136:139], v[80:95]
	ds_read_b64_tr_b16 v[200:201], v177 offset:0x4600
	ds_read_b64_tr_b16 v[202:203], v177 offset:0x5600
	s_waitcnt lgkmcnt(6)
	v_mfma_f32_32x32x16_bf16 v[80:95], v[156:159], v[140:143], v[80:95]
	ds_read_b64_tr_b16 v[204:205], v177 offset:0x6600
	ds_read_b64_tr_b16 v[206:207], v177 offset:0x7600
	s_waitcnt lgkmcnt(6)
	v_mfma_f32_32x32x16_bf16 v[64:79], v[192:195], v[128:131], v[64:79]
	ds_read_b64_tr_b16 v[144:145], v177 offset:0x800
	ds_read_b64_tr_b16 v[146:147], v177 offset:0x1800
	s_waitcnt lgkmcnt(6)
	v_mfma_f32_32x32x16_bf16 v[64:79], v[196:199], v[132:135], v[64:79]
	ds_read_b64_tr_b16 v[148:149], v177 offset:0x2800
	ds_read_b64_tr_b16 v[150:151], v177 offset:0x3800
	s_waitcnt lgkmcnt(6)
	v_mfma_f32_32x32x16_bf16 v[64:79], v[200:203], v[136:139], v[64:79]
	ds_read_b64_tr_b16 v[152:153], v177 offset:0x4800
	ds_read_b64_tr_b16 v[154:155], v177 offset:0x5800
	s_waitcnt lgkmcnt(6)
	v_mfma_f32_32x32x16_bf16 v[64:79], v[204:207], v[140:143], v[64:79]
	ds_read_b64_tr_b16 v[156:157], v177 offset:0x6800
	ds_read_b64_tr_b16 v[158:159], v177 offset:0x7800
	s_waitcnt lgkmcnt(6)
	v_mfma_f32_32x32x16_bf16 v[48:63], v[144:147], v[128:131], v[48:63]
	ds_read_b64_tr_b16 v[192:193], v177 offset:0xa00
	ds_read_b64_tr_b16 v[194:195], v177 offset:0x1a00
	s_waitcnt lgkmcnt(6)
	v_mfma_f32_32x32x16_bf16 v[48:63], v[148:151], v[132:135], v[48:63]
	ds_read_b64_tr_b16 v[196:197], v177 offset:0x2a00
	ds_read_b64_tr_b16 v[198:199], v177 offset:0x3a00
	s_waitcnt lgkmcnt(6)
	v_mfma_f32_32x32x16_bf16 v[48:63], v[152:155], v[136:139], v[48:63]
	ds_read_b64_tr_b16 v[200:201], v177 offset:0x4a00
	ds_read_b64_tr_b16 v[202:203], v177 offset:0x5a00
	s_waitcnt lgkmcnt(6)
	v_mfma_f32_32x32x16_bf16 v[48:63], v[156:159], v[140:143], v[48:63]
	ds_read_b64_tr_b16 v[204:205], v177 offset:0x6a00
	ds_read_b64_tr_b16 v[206:207], v177 offset:0x7a00
	s_waitcnt lgkmcnt(6)
	v_mfma_f32_32x32x16_bf16 v[32:47], v[192:195], v[128:131], v[32:47]
	ds_read_b64_tr_b16 v[144:145], v177 offset:0xc00
	ds_read_b64_tr_b16 v[146:147], v177 offset:0x1c00
	s_waitcnt lgkmcnt(6)
	v_mfma_f32_32x32x16_bf16 v[32:47], v[196:199], v[132:135], v[32:47]
	ds_read_b64_tr_b16 v[148:149], v177 offset:0x2c00
	ds_read_b64_tr_b16 v[150:151], v177 offset:0x3c00
	s_waitcnt lgkmcnt(6)
	v_mfma_f32_32x32x16_bf16 v[32:47], v[200:203], v[136:139], v[32:47]
	ds_read_b64_tr_b16 v[152:153], v177 offset:0x4c00
	ds_read_b64_tr_b16 v[154:155], v177 offset:0x5c00
	s_waitcnt lgkmcnt(6)
	v_mfma_f32_32x32x16_bf16 v[32:47], v[204:207], v[140:143], v[32:47]
	ds_read_b64_tr_b16 v[156:157], v177 offset:0x6c00
	ds_read_b64_tr_b16 v[158:159], v177 offset:0x7c00
	s_waitcnt lgkmcnt(6)
	v_mfma_f32_32x32x16_bf16 v[16:31], v[144:147], v[128:131], v[16:31]
	ds_read_b64_tr_b16 v[192:193], v177 offset:0xe00
	ds_read_b64_tr_b16 v[194:195], v177 offset:0x1e00
	s_waitcnt lgkmcnt(6)
	v_mfma_f32_32x32x16_bf16 v[16:31], v[148:151], v[132:135], v[16:31]
	ds_read_b64_tr_b16 v[196:197], v177 offset:0x2e00
	ds_read_b64_tr_b16 v[198:199], v177 offset:0x3e00
	s_waitcnt lgkmcnt(6)
	v_mfma_f32_32x32x16_bf16 v[16:31], v[152:155], v[136:139], v[16:31]
	ds_read_b64_tr_b16 v[200:201], v177 offset:0x4e00
	ds_read_b64_tr_b16 v[202:203], v177 offset:0x5e00
	s_waitcnt lgkmcnt(6)
	v_mfma_f32_32x32x16_bf16 v[16:31], v[156:159], v[140:143], v[16:31]
	ds_read_b64_tr_b16 v[204:205], v177 offset:0x6e00
	ds_read_b64_tr_b16 v[206:207], v177 offset:0x7e00
	s_waitcnt lgkmcnt(6)
	v_mfma_f32_32x32x16_bf16 v[0:15], v[192:195], v[128:131], v[0:15]
	s_waitcnt lgkmcnt(4)
	v_mfma_f32_32x32x16_bf16 v[0:15], v[196:199], v[132:135], v[0:15]
	s_waitcnt lgkmcnt(2)
	v_mfma_f32_32x32x16_bf16 v[0:15], v[200:203], v[136:139], v[0:15]
	s_waitcnt lgkmcnt(0)
	v_mfma_f32_32x32x16_bf16 v[0:15], v[204:207], v[140:143], v[0:15]
	ds_read_b128 v[128:131], v188 offset:0
	ds_read_b128 v[132:135], v188 offset:0x2000
	ds_read_b128 v[192:195], v187 offset:0
	ds_read_b128 v[196:199], v187 offset:0x2000
	s_waitcnt lgkmcnt(2)
	s_nop 0
	v_mfma_f32_32x32x16_bf16 v[144:159], v[128:131], v[218:221], 0
	v_mfma_f32_32x32x16_bf16 v[128:143], v[132:135], v[218:221], 0
	ds_read_b128 v[204:207], v186 offset:0
	ds_read_b128 v[208:211], v186 offset:0x2000
	s_waitcnt lgkmcnt(2)
	v_mfma_f32_32x32x16_bf16 v[144:159], v[192:195], v[222:225], v[144:159]
	v_mfma_f32_32x32x16_bf16 v[128:143], v[196:199], v[222:225], v[128:143]
	ds_read_b128 v[192:195], v185 offset:0
	ds_read_b128 v[196:199], v185 offset:0x2000
	s_waitcnt lgkmcnt(2)
	v_mfma_f32_32x32x16_bf16 v[144:159], v[204:207], v[230:233], v[144:159]
	v_mfma_f32_32x32x16_bf16 v[128:143], v[208:211], v[230:233], v[128:143]
	ds_read_b128 v[204:207], v188 offset:0x80
	ds_read_b128 v[208:211], v188 offset:0x2080
	s_waitcnt lgkmcnt(2)
	v_mfma_f32_32x32x16_bf16 v[144:159], v[192:195], v[234:237], v[144:159]
	v_mfma_f32_32x32x16_bf16 v[128:143], v[196:199], v[234:237], v[128:143]
	ds_read_b128 v[192:195], v187 offset:0x80
	ds_read_b128 v[196:199], v187 offset:0x2080
	s_waitcnt lgkmcnt(2)
	v_mfma_f32_32x32x16_bf16 v[144:159], v[204:207], v[238:241], v[144:159]
	v_mfma_f32_32x32x16_bf16 v[128:143], v[208:211], v[238:241], v[128:143]
	ds_read_b128 v[204:207], v186 offset:0x80
	ds_read_b128 v[208:211], v186 offset:0x2080
	s_waitcnt lgkmcnt(2)
	v_mfma_f32_32x32x16_bf16 v[144:159], v[192:195], v[242:245], v[144:159]
	v_mfma_f32_32x32x16_bf16 v[128:143], v[196:199], v[242:245], v[128:143]
	ds_read_b128 v[192:195], v185 offset:0x80
	ds_read_b128 v[196:199], v185 offset:0x2080
	s_waitcnt lgkmcnt(2)
	v_mfma_f32_32x32x16_bf16 v[144:159], v[204:207], v[246:249], v[144:159]
	v_mfma_f32_32x32x16_bf16 v[128:143], v[208:211], v[246:249], v[128:143]
	s_waitcnt lgkmcnt(0)
	s_bitcmp0_b32 s100, 8
	s_cbranch_scc1 .Lqk7bar_2
	s_waitcnt vmcnt(0)
	s_barrier

.LBB0_597:
	ds_read_b64_tr_b16 v[144:145], v177 offset:0x8000
	ds_read_b64_tr_b16 v[146:147], v177 offset:0x9000
	ds_read_b64_tr_b16 v[148:149], v177 offset:0xa000
	ds_read_b64_tr_b16 v[150:151], v177 offset:0xb000
	ds_read_b64_tr_b16 v[152:153], v177 offset:0xc000
	ds_read_b64_tr_b16 v[154:155], v177 offset:0xd000
	ds_read_b64_tr_b16 v[156:157], v177 offset:0xe000
	ds_read_b64_tr_b16 v[158:159], v177 offset:0xf000
	s_waitcnt lgkmcnt(6)
	s_nop 0
	v_mfma_f32_32x32x16_bf16 v[112:127], v[144:147], v[128:131], v[112:127]
	ds_read_b64_tr_b16 v[194:195], v177 offset:0x8200
	ds_read_b64_tr_b16 v[196:197], v177 offset:0x9200
	s_waitcnt lgkmcnt(6)
	v_mfma_f32_32x32x16_bf16 v[112:127], v[148:151], v[132:135], v[112:127]
	ds_read_b64_tr_b16 v[198:199], v177 offset:0xa200
	ds_read_b64_tr_b16 v[200:201], v177 offset:0xb200
	s_waitcnt lgkmcnt(6)
	v_mfma_f32_32x32x16_bf16 v[112:127], v[152:155], v[136:139], v[112:127]
	ds_read_b64_tr_b16 v[202:203], v177 offset:0xc200
	ds_read_b64_tr_b16 v[204:205], v177 offset:0xd200
	s_waitcnt lgkmcnt(6)
	v_mfma_f32_32x32x16_bf16 v[112:127], v[156:159], v[140:143], v[112:127]
	ds_read_b64_tr_b16 v[206:207], v177 offset:0xe200
	ds_read_b64_tr_b16 v[208:209], v177 offset:0xf200
	s_waitcnt lgkmcnt(6)
	v_mfma_f32_32x32x16_bf16 v[96:111], v[194:197], v[128:131], v[96:111]
	ds_read_b64_tr_b16 v[144:145], v177 offset:0x8400
	ds_read_b64_tr_b16 v[146:147], v177 offset:0x9400
	s_waitcnt lgkmcnt(6)
	v_mfma_f32_32x32x16_bf16 v[96:111], v[198:201], v[132:135], v[96:111]
	ds_read_b64_tr_b16 v[148:149], v177 offset:0xa400
	ds_read_b64_tr_b16 v[150:151], v177 offset:0xb400
	s_waitcnt lgkmcnt(6)
	v_mfma_f32_32x32x16_bf16 v[96:111], v[202:205], v[136:139], v[96:111]
	ds_read_b64_tr_b16 v[152:153], v177 offset:0xc400
	ds_read_b64_tr_b16 v[154:155], v177 offset:0xd400
	s_waitcnt lgkmcnt(6)
	v_mfma_f32_32x32x16_bf16 v[96:111], v[206:209], v[140:143], v[96:111]
	ds_read_b64_tr_b16 v[156:157], v177 offset:0xe400
	ds_read_b64_tr_b16 v[158:159], v177 offset:0xf400
	s_waitcnt lgkmcnt(6)
	v_mfma_f32_32x32x16_bf16 v[80:95], v[144:147], v[128:131], v[80:95]
	ds_read_b64_tr_b16 v[194:195], v177 offset:0x8600
	ds_read_b64_tr_b16 v[196:197], v177 offset:0x9600
	s_waitcnt lgkmcnt(6)
	v_mfma_f32_32x32x16_bf16 v[80:95], v[148:151], v[132:135], v[80:95]
	ds_read_b64_tr_b16 v[198:199], v177 offset:0xa600
	ds_read_b64_tr_b16 v[200:201], v177 offset:0xb600
	s_waitcnt lgkmcnt(6)
	v_mfma_f32_32x32x16_bf16 v[80:95], v[152:155], v[136:139], v[80:95]
	ds_read_b64_tr_b16 v[202:203], v177 offset:0xc600
	ds_read_b64_tr_b16 v[204:205], v177 offset:0xd600
	s_waitcnt lgkmcnt(6)
	v_mfma_f32_32x32x16_bf16 v[80:95], v[156:159], v[140:143], v[80:95]
	ds_read_b64_tr_b16 v[206:207], v177 offset:0xe600
	ds_read_b64_tr_b16 v[208:209], v177 offset:0xf600
	s_waitcnt lgkmcnt(6)
	v_mfma_f32_32x32x16_bf16 v[64:79], v[194:197], v[128:131], v[64:79]
	ds_read_b64_tr_b16 v[144:145], v177 offset:0x8800
	ds_read_b64_tr_b16 v[146:147], v177 offset:0x9800
	s_waitcnt lgkmcnt(6)
	v_mfma_f32_32x32x16_bf16 v[64:79], v[198:201], v[132:135], v[64:79]
	ds_read_b64_tr_b16 v[148:149], v177 offset:0xa800
	ds_read_b64_tr_b16 v[150:151], v177 offset:0xb800
	s_waitcnt lgkmcnt(6)
	v_mfma_f32_32x32x16_bf16 v[64:79], v[202:205], v[136:139], v[64:79]
	ds_read_b64_tr_b16 v[152:153], v177 offset:0xc800
	ds_read_b64_tr_b16 v[154:155], v177 offset:0xd800
	s_waitcnt lgkmcnt(6)
	v_mfma_f32_32x32x16_bf16 v[64:79], v[206:209], v[140:143], v[64:79]
	ds_read_b64_tr_b16 v[156:157], v177 offset:0xe800
	ds_read_b64_tr_b16 v[158:159], v177 offset:0xf800
	s_waitcnt lgkmcnt(6)
	v_mfma_f32_32x32x16_bf16 v[48:63], v[144:147], v[128:131], v[48:63]
	ds_read_b64_tr_b16 v[194:195], v177 offset:0x8a00
	ds_read_b64_tr_b16 v[196:197], v177 offset:0x9a00
	s_waitcnt lgkmcnt(6)
	v_mfma_f32_32x32x16_bf16 v[48:63], v[148:151], v[132:135], v[48:63]
	ds_read_b64_tr_b16 v[198:199], v177 offset:0xaa00
	ds_read_b64_tr_b16 v[200:201], v177 offset:0xba00
	s_waitcnt lgkmcnt(6)
	v_mfma_f32_32x32x16_bf16 v[48:63], v[152:155], v[136:139], v[48:63]
	ds_read_b64_tr_b16 v[202:203], v177 offset:0xca00
	ds_read_b64_tr_b16 v[204:205], v177 offset:0xda00
	s_waitcnt lgkmcnt(6)
	v_mfma_f32_32x32x16_bf16 v[48:63], v[156:159], v[140:143], v[48:63]
	ds_read_b64_tr_b16 v[206:207], v177 offset:0xea00
	ds_read_b64_tr_b16 v[208:209], v177 offset:0xfa00
	s_waitcnt lgkmcnt(6)
	v_mfma_f32_32x32x16_bf16 v[32:47], v[194:197], v[128:131], v[32:47]
	ds_read_b64_tr_b16 v[144:145], v177 offset:0x8c00
	ds_read_b64_tr_b16 v[146:147], v177 offset:0x9c00
	s_waitcnt lgkmcnt(6)
	v_mfma_f32_32x32x16_bf16 v[32:47], v[198:201], v[132:135], v[32:47]
	ds_read_b64_tr_b16 v[148:149], v177 offset:0xac00
	ds_read_b64_tr_b16 v[150:151], v177 offset:0xbc00
	s_waitcnt lgkmcnt(6)
	v_mfma_f32_32x32x16_bf16 v[32:47], v[202:205], v[136:139], v[32:47]
	ds_read_b64_tr_b16 v[152:153], v177 offset:0xcc00
	ds_read_b64_tr_b16 v[154:155], v177 offset:0xdc00
	s_waitcnt lgkmcnt(6)
	v_mfma_f32_32x32x16_bf16 v[32:47], v[206:209], v[140:143], v[32:47]
	ds_read_b64_tr_b16 v[156:157], v177 offset:0xec00
	ds_read_b64_tr_b16 v[158:159], v177 offset:0xfc00
	s_waitcnt lgkmcnt(6)
	v_mfma_f32_32x32x16_bf16 v[16:31], v[144:147], v[128:131], v[16:31]
	ds_read_b64_tr_b16 v[194:195], v177 offset:0x8e00
	ds_read_b64_tr_b16 v[196:197], v177 offset:0x9e00
	s_waitcnt lgkmcnt(6)
	v_mfma_f32_32x32x16_bf16 v[16:31], v[148:151], v[132:135], v[16:31]
	ds_read_b64_tr_b16 v[198:199], v177 offset:0xae00
	ds_read_b64_tr_b16 v[200:201], v177 offset:0xbe00
	s_waitcnt lgkmcnt(6)
	v_mfma_f32_32x32x16_bf16 v[16:31], v[152:155], v[136:139], v[16:31]
	ds_read_b64_tr_b16 v[202:203], v177 offset:0xce00
	ds_read_b64_tr_b16 v[204:205], v177 offset:0xde00
	s_waitcnt lgkmcnt(6)
	v_mfma_f32_32x32x16_bf16 v[16:31], v[156:159], v[140:143], v[16:31]
	ds_read_b64_tr_b16 v[206:207], v177 offset:0xee00
	ds_read_b64_tr_b16 v[208:209], v177 offset:0xfe00
	s_waitcnt lgkmcnt(6)
	v_mfma_f32_32x32x16_bf16 v[0:15], v[194:197], v[128:131], v[0:15]
	s_waitcnt lgkmcnt(4)
	v_mfma_f32_32x32x16_bf16 v[0:15], v[198:201], v[132:135], v[0:15]
	s_waitcnt lgkmcnt(2)
	v_mfma_f32_32x32x16_bf16 v[0:15], v[202:205], v[136:139], v[0:15]
	s_waitcnt lgkmcnt(0)
	v_mfma_f32_32x32x16_bf16 v[0:15], v[206:209], v[140:143], v[0:15]
	ds_read_b128 v[128:131], v181 offset:0
	ds_read_b128 v[132:135], v181 offset:0x2000
	ds_read_b128 v[194:197], v182 offset:0
	ds_read_b128 v[198:201], v182 offset:0x2000
	s_waitcnt lgkmcnt(2)
	s_nop 0
	v_mfma_f32_32x32x16_bf16 v[144:159], v[128:131], v[218:221], 0
	v_mfma_f32_32x32x16_bf16 v[128:143], v[132:135], v[218:221], 0
	ds_read_b128 v[206:209], v183 offset:0
	ds_read_b128 v[210:213], v183 offset:0x2000
	s_waitcnt lgkmcnt(2)
	v_mfma_f32_32x32x16_bf16 v[144:159], v[194:197], v[222:225], v[144:159]
	v_mfma_f32_32x32x16_bf16 v[128:143], v[198:201], v[222:225], v[128:143]
	ds_read_b128 v[194:197], v184 offset:0
	ds_read_b128 v[198:201], v184 offset:0x2000
	s_waitcnt lgkmcnt(2)
	v_mfma_f32_32x32x16_bf16 v[144:159], v[206:209], v[230:233], v[144:159]
	v_mfma_f32_32x32x16_bf16 v[128:143], v[210:213], v[230:233], v[128:143]
	ds_read_b128 v[206:209], v181 offset:0x80
	ds_read_b128 v[210:213], v181 offset:0x2080
	s_waitcnt lgkmcnt(2)
	v_mfma_f32_32x32x16_bf16 v[144:159], v[194:197], v[234:237], v[144:159]
	v_mfma_f32_32x32x16_bf16 v[128:143], v[198:201], v[234:237], v[128:143]
	ds_read_b128 v[194:197], v182 offset:0x80
	ds_read_b128 v[198:201], v182 offset:0x2080
	s_waitcnt lgkmcnt(2)
	v_mfma_f32_32x32x16_bf16 v[144:159], v[206:209], v[238:241], v[144:159]
	v_mfma_f32_32x32x16_bf16 v[128:143], v[210:213], v[238:241], v[128:143]
	ds_read_b128 v[206:209], v183 offset:0x80
	ds_read_b128 v[210:213], v183 offset:0x2080
	s_waitcnt lgkmcnt(2)
	v_mfma_f32_32x32x16_bf16 v[144:159], v[194:197], v[242:245], v[144:159]
	v_mfma_f32_32x32x16_bf16 v[128:143], v[198:201], v[242:245], v[128:143]
	ds_read_b128 v[194:197], v184 offset:0x80
	ds_read_b128 v[198:201], v184 offset:0x2080
	s_waitcnt lgkmcnt(2)
	v_mfma_f32_32x32x16_bf16 v[144:159], v[206:209], v[246:249], v[144:159]
	v_mfma_f32_32x32x16_bf16 v[128:143], v[210:213], v[246:249], v[128:143]
	s_waitcnt lgkmcnt(0)
	s_bitcmp0_b32 s100, 8
	s_cbranch_scc1 .Lqk7bar_3
	s_waitcnt vmcnt(0)
	s_barrier
